# C1 + P0 rebalance: workgroups with two weight column groups hand one rmsnorm row per wave to the lighter half (15 vs 17 rows)
# speedup vs baseline: 1.0033x; 1.0033x over previous
.LBB0_39:
	s_or_b64 exec, exec, s[4:5]
	s_cmp_lt_i32 s40, 0x8000
	s_cbranch_scc0 .LBB0_44
	v_readlane_b32 s2, v255, 9
	v_readlane_b32 s3, v255, 10
	s_load_dwordx2 s[4:5], s[2:3], 0x8
	v_ashrrev_i32_e32 v35, 31, v34
	v_lshlrev_b64 v[36:37], 2, v[34:35]
	s_movk_i32 s3, 0x1000
	s_ashr_i32 s41, s40, 31
	s_waitcnt lgkmcnt(0)
	v_lshl_add_u64 v[26:27], s[4:5], 0, v[36:37]
	global_load_dwordx4 v[2:5], v[26:27], off offset:16
	global_load_dwordx4 v[6:9], v[26:27], off
	global_load_dwordx4 v[10:13], v[26:27], off offset:2064
	global_load_dwordx4 v[14:17], v[26:27], off offset:2048
	s_mov_b64 s[4:5], 0x1000
	v_add_co_u32_e32 v38, vcc, s3, v26
	v_lshl_add_u64 v[28:29], v[26:27], 0, s[4:5]
	s_nop 0
	v_addc_co_u32_e32 v39, vcc, 0, v27, vcc
	s_mov_b64 s[4:5], 0x1800
	global_load_dwordx4 v[18:21], v[38:39], off
	global_load_dwordx4 v[22:25], v[28:29], off offset:16
	v_lshl_add_u64 v[40:41], v[26:27], 0, s[4:5]
	global_load_dwordx4 v[26:29], v[38:39], off offset:2048
	global_load_dwordx4 v[30:33], v[40:41], off offset:16
	v_and_b32_e32 v38, 64, v254
	v_add_u32_e32 v38, 64, v38
	v_xor_b32_e32 v39, 1, v254
	v_cmp_lt_i32_e32 vcc, v39, v38
	s_lshl_b64 s[4:5], s[40:41], 2
	s_add_u32 s3, s4, 0x4910000
	v_cndmask_b32_e32 v39, v254, v39, vcc
	v_lshlrev_b32_e32 v70, 2, v39
	v_xor_b32_e32 v39, 2, v254
	v_cmp_lt_i32_e32 vcc, v39, v38
	s_addc_u32 s16, s5, 0
	s_ashr_i32 s91, s90, 31
	v_cndmask_b32_e32 v39, v254, v39, vcc
	v_lshlrev_b32_e32 v71, 2, v39
	v_xor_b32_e32 v39, 4, v254
	v_cmp_lt_i32_e32 vcc, v39, v38
	s_lshl_b64 s[8:9], s[40:41], 11
	s_lshl_b64 s[4:5], s[90:91], 2
	v_cndmask_b32_e32 v39, v254, v39, vcc
	v_lshlrev_b32_e32 v72, 2, v39
	v_xor_b32_e32 v39, 8, v254
	v_cmp_lt_i32_e32 vcc, v39, v38
	s_lshl_b64 s[10:11], s[90:91], 11
	v_readlane_b32 s12, v255, 11
	v_cndmask_b32_e32 v39, v254, v39, vcc
	v_lshlrev_b32_e32 v73, 2, v39
	v_xor_b32_e32 v39, 16, v254
	v_cmp_lt_i32_e32 vcc, v39, v38
	v_readlane_b32 s13, v255, 12
	s_movk_i32 s14, 0xe7f0
	v_cndmask_b32_e32 v39, v254, v39, vcc
	v_lshlrev_b32_e32 v74, 2, v39
	v_xor_b32_e32 v39, 32, v254
	v_cmp_lt_i32_e32 vcc, v39, v38
	v_cmp_eq_u32_e64 s[6:7], 0, v1
	s_mov_b32 s15, -1
	v_cndmask_b32_e32 v38, v254, v39, vcc
	v_lshlrev_b32_e32 v75, 2, v38
	v_lshl_add_u64 v[38:39], s[8:9], 0, v[34:35]
	s_lshl_b64 s[8:9], s[40:41], 13
	s_add_u32 s8, s12, s8
	s_addc_u32 s9, s13, s9
	v_lshl_add_u64 v[34:35], s[8:9], 0, v[36:37]
	s_mov_b64 s[8:9], 0x1810
	v_lshl_add_u64 v[40:41], v[34:35], 0, s[8:9]
	s_lshl_b64 s[12:13], s[90:91], 13
	v_mov_b32_e32 v1, 0x358637bd
	s_mov_b32 s17, 0xf800000
	v_mov_b32_e32 v76, 0x260
	v_mov_b32_e32 v77, 0
	s_mov_b32 s18, 0x42fe0000
	s_mov_b32 s19, 0xc2fe0000
	s_mov_b32 s20, 0x40c0c00
	s_mov_b32 s21, 0x39000000
	v_mov_b32_e32 v78, 0x42fe0000
	s_mov_b32 s22, s40
	s_mov_b32 s32, 0x8000
	s_cmp_lt_i32 s40, 0x400
	s_cselect_b32 s32, 0x7800, s32
	s_branch .LBB0_42
.LBB0_41:
	s_or_b64 exec, exec, s[8:9]
	v_div_scale_f32 v80, s[8:9], v79, v79, s18
	v_rcp_f32_e32 v81, v80
	v_div_scale_f32 v82, vcc, s18, v79, s18
	s_add_i32 s22, s22, s90
	v_fma_f32 v83, -v80, v81, 1.0
	v_fmac_f32_e32 v81, v83, v81
	v_mul_f32_e32 v83, v82, v81
	v_fma_f32 v84, -v80, v83, v82
	v_fmac_f32_e32 v83, v84, v81
	v_fma_f32 v80, -v80, v83, v82
	v_div_fmas_f32 v80, v80, v81, v83
	v_div_fixup_f32 v80, v80, v79, s18
	v_cmp_lt_f32_e32 vcc, 0, v79
	v_lshl_add_u64 v[82:83], s[26:27], 0, v[38:39]
	s_add_u32 s3, s3, s4
	v_cndmask_b32_e32 v80, 0, v80, vcc
	v_pk_mul_f32 v[44:45], v[80:81], v[44:45] op_sel_hi:[0,1]
	v_pk_mul_f32 v[36:37], v[80:81], v[36:37] op_sel_hi:[0,1]
	v_rndne_f32_e32 v45, v45
	v_rndne_f32_e32 v44, v44
	v_med3_f32 v45, v45, s19, v78
	v_rndne_f32_e32 v36, v36
	v_rndne_f32_e32 v37, v37
	v_med3_f32 v44, v44, s19, v78
	v_cvt_i32_f32_e32 v45, v45
	v_med3_f32 v36, v36, s19, v78
	v_med3_f32 v37, v37, s19, v78
	v_cvt_i32_f32_e32 v44, v44
	v_cvt_i32_f32_sdwa v36, v36 dst_sel:WORD_1 dst_unused:UNUSED_PAD src0_sel:DWORD
	v_cvt_i32_f32_e32 v37, v37
	v_pk_mul_f32 v[68:69], v[80:81], v[68:69] op_sel_hi:[0,1]
	v_pk_mul_f32 v[64:65], v[80:81], v[64:65] op_sel_hi:[0,1]
	v_lshlrev_b32_e32 v45, 8, v45
	v_pk_mul_f32 v[66:67], v[80:81], v[66:67] op_sel_hi:[0,1]
	v_pk_mul_f32 v[62:63], v[80:81], v[62:63] op_sel_hi:[0,1]
	v_rndne_f32_e32 v69, v69
	v_rndne_f32_e32 v65, v65
	v_pk_mul_f32 v[60:61], v[80:81], v[60:61] op_sel_hi:[0,1]
	v_pk_mul_f32 v[56:57], v[80:81], v[56:57] op_sel_hi:[0,1]
	v_pk_mul_f32 v[52:53], v[80:81], v[52:53] op_sel_hi:[0,1]
	v_pk_mul_f32 v[48:49], v[80:81], v[48:49] op_sel_hi:[0,1]
	v_pk_mul_f32 v[42:43], v[80:81], v[42:43] op_sel_hi:[0,1]
	v_and_b32_e32 v45, 0xff00, v45
	v_and_b32_e32 v36, 0xff0000, v36
	v_perm_b32 v37, v37, v44, s20
	v_rndne_f32_e32 v68, v68
	v_med3_f32 v69, v69, s19, v78
	v_rndne_f32_e32 v66, v66
	v_rndne_f32_e32 v67, v67
	v_rndne_f32_e32 v64, v64
	v_med3_f32 v65, v65, s19, v78
	v_rndne_f32_e32 v62, v62
	v_rndne_f32_e32 v63, v63
	v_pk_mul_f32 v[58:59], v[80:81], v[58:59] op_sel_hi:[0,1]
	v_pk_mul_f32 v[54:55], v[80:81], v[54:55] op_sel_hi:[0,1]
	v_rndne_f32_e32 v61, v61
	v_rndne_f32_e32 v57, v57
	v_pk_mul_f32 v[50:51], v[80:81], v[50:51] op_sel_hi:[0,1]
	v_pk_mul_f32 v[46:47], v[80:81], v[46:47] op_sel_hi:[0,1]
	v_rndne_f32_e32 v53, v53
	v_rndne_f32_e32 v49, v49
	v_pk_mul_f32 v[34:35], v[80:81], v[34:35] op_sel_hi:[0,1]
	v_or3_b32 v36, v37, v45, v36
	v_rndne_f32_e32 v37, v42
	v_rndne_f32_e32 v42, v43
	v_med3_f32 v68, v68, s19, v78
	v_cvt_i32_f32_e32 v69, v69
	v_med3_f32 v66, v66, s19, v78
	v_med3_f32 v67, v67, s19, v78
	v_med3_f32 v64, v64, s19, v78
	v_cvt_i32_f32_e32 v65, v65
	v_med3_f32 v62, v62, s19, v78
	v_med3_f32 v63, v63, s19, v78
	v_rndne_f32_e32 v60, v60
	v_med3_f32 v61, v61, s19, v78
	v_rndne_f32_e32 v58, v58
	v_rndne_f32_e32 v59, v59
	v_rndne_f32_e32 v56, v56
	v_med3_f32 v57, v57, s19, v78
	v_rndne_f32_e32 v54, v54
	v_rndne_f32_e32 v55, v55
	v_rndne_f32_e32 v52, v52
	v_med3_f32 v53, v53, s19, v78
	v_rndne_f32_e32 v50, v50
	v_rndne_f32_e32 v51, v51
	v_rndne_f32_e32 v48, v48
	v_med3_f32 v49, v49, s19, v78
	v_rndne_f32_e32 v46, v46
	v_rndne_f32_e32 v47, v47
	v_med3_f32 v42, v42, s19, v78
	v_rndne_f32_e32 v34, v34
	v_rndne_f32_e32 v35, v35
	v_cvt_i32_f32_e32 v68, v68
	v_cvt_i32_f32_sdwa v66, v66 dst_sel:WORD_1 dst_unused:UNUSED_PAD src0_sel:DWORD
	v_cvt_i32_f32_e32 v67, v67
	v_cvt_i32_f32_e32 v64, v64
	v_cvt_i32_f32_sdwa v62, v62 dst_sel:WORD_1 dst_unused:UNUSED_PAD src0_sel:DWORD
	v_cvt_i32_f32_e32 v63, v63
	v_med3_f32 v60, v60, s19, v78
	v_cvt_i32_f32_e32 v61, v61
	v_med3_f32 v58, v58, s19, v78
	v_med3_f32 v59, v59, s19, v78
	v_med3_f32 v56, v56, s19, v78
	v_cvt_i32_f32_e32 v57, v57
	v_med3_f32 v54, v54, s19, v78
	v_med3_f32 v55, v55, s19, v78
	v_med3_f32 v52, v52, s19, v78
	v_cvt_i32_f32_e32 v53, v53
	v_med3_f32 v50, v50, s19, v78
	v_med3_f32 v51, v51, s19, v78
	v_med3_f32 v48, v48, s19, v78
	v_cvt_i32_f32_e32 v49, v49
	v_med3_f32 v46, v46, s19, v78
	v_med3_f32 v47, v47, s19, v78
	v_med3_f32 v37, v37, s19, v78
	v_cvt_i32_f32_e32 v42, v42
	v_med3_f32 v34, v34, s19, v78
	v_med3_f32 v35, v35, s19, v78
	v_cvt_i32_f32_e32 v60, v60
	v_cvt_i32_f32_sdwa v58, v58 dst_sel:WORD_1 dst_unused:UNUSED_PAD src0_sel:DWORD
	v_cvt_i32_f32_e32 v59, v59
	v_cvt_i32_f32_e32 v56, v56
	v_cvt_i32_f32_sdwa v54, v54 dst_sel:WORD_1 dst_unused:UNUSED_PAD src0_sel:DWORD
	v_cvt_i32_f32_e32 v55, v55
	v_cvt_i32_f32_e32 v52, v52
	v_cvt_i32_f32_sdwa v50, v50 dst_sel:WORD_1 dst_unused:UNUSED_PAD src0_sel:DWORD
	v_cvt_i32_f32_e32 v51, v51
	v_cvt_i32_f32_e32 v48, v48
	v_cvt_i32_f32_sdwa v46, v46 dst_sel:WORD_1 dst_unused:UNUSED_PAD src0_sel:DWORD
	v_cvt_i32_f32_e32 v47, v47
	v_cvt_i32_f32_e32 v37, v37
	v_cvt_i32_f32_sdwa v34, v34 dst_sel:WORD_1 dst_unused:UNUSED_PAD src0_sel:DWORD
	v_cvt_i32_f32_e32 v35, v35
	v_lshlrev_b32_e32 v69, 8, v69
	v_lshlrev_b32_e32 v65, 8, v65
	v_and_b32_e32 v69, 0xff00, v69
	v_and_b32_e32 v66, 0xff0000, v66
	v_perm_b32 v67, v67, v68, s20
	v_and_b32_e32 v65, 0xff00, v65
	v_and_b32_e32 v62, 0xff0000, v62
	v_perm_b32 v63, v63, v64, s20
	v_lshlrev_b32_e32 v61, 8, v61
	v_lshlrev_b32_e32 v57, 8, v57
	v_lshlrev_b32_e32 v53, 8, v53
	v_lshlrev_b32_e32 v49, 8, v49
	v_lshlrev_b32_e32 v42, 8, v42
	v_or3_b32 v66, v67, v69, v66
	v_or3_b32 v67, v63, v65, v62
	v_add_co_u32_e32 v62, vcc, s21, v82
	v_and_b32_e32 v61, 0xff00, v61
	v_and_b32_e32 v58, 0xff0000, v58
	v_perm_b32 v59, v59, v60, s20
	v_and_b32_e32 v57, 0xff00, v57
	v_and_b32_e32 v54, 0xff0000, v54
	v_perm_b32 v55, v55, v56, s20
	v_and_b32_e32 v53, 0xff00, v53
	v_and_b32_e32 v50, 0xff0000, v50
	v_perm_b32 v51, v51, v52, s20
	v_and_b32_e32 v49, 0xff00, v49
	v_and_b32_e32 v46, 0xff0000, v46
	v_perm_b32 v47, v47, v48, s20
	v_and_b32_e32 v42, 0xff00, v42
	v_and_b32_e32 v34, 0xff0000, v34
	v_perm_b32 v35, v35, v37, s20
	s_addc_u32 s16, s16, s5
	v_addc_co_u32_e32 v63, vcc, 0, v83, vcc
	v_or3_b32 v58, v59, v61, v58
	v_or3_b32 v59, v55, v57, v54
	v_or3_b32 v50, v51, v53, v50
	v_or3_b32 v51, v47, v49, v46
	v_or3_b32 v37, v35, v42, v34
	v_lshl_add_u64 v[38:39], v[38:39], 0, s[10:11]
	s_cmp_lt_i32 s22, s32
	v_lshl_add_u64 v[40:41], v[40:41], 0, s[12:13]
	global_store_dwordx2 v[62:63], v[66:67], off
	global_store_dwordx2 v[62:63], v[58:59], off offset:512
	global_store_dwordx2 v[62:63], v[50:51], off offset:1024
	global_store_dwordx2 v[62:63], v[36:37], off offset:1536
	s_cbranch_scc0 .Lrb0_tail

.Lrb0_tail:
	s_cmp_eq_u32 s32, 0x8000
	s_cbranch_scc0 .LBB0_44
	s_mov_b32 s32, 0
	s_add_u32 s3, s3, 0xffffd000
	s_addc_u32 s16, s16, -1
	s_mov_b32 s24, 0xffa00000
	s_mov_b32 s25, -1
	v_lshl_add_u64 v[38:39], v[38:39], 0, s[24:25]
	s_mov_b32 s24, 0xfe800000
	s_nop 0
	v_lshl_add_u64 v[40:41], v[40:41], 0, s[24:25]
	s_branch .LBB0_42
